# speedup vs baseline: 1.0192x; 1.0192x over previous
.Lk5_epi:
	v_lshlrev_b32_e32 v64, 1, v48
	global_load_dwordx4 v[0:3], v64, s[6:7]
	global_load_dwordx4 v[4:7], v64, s[6:7] offset:16
	v_div_scale_f32 v65, s[2:3], v53, v53, 1.0
	v_rcp_f32_e32 v66, v65
	v_min_i32_e32 v68, 0xc34f, v49
	v_lshlrev_b32_e32 v68, 8, v68
	v_fma_f32 v62, -v65, v66, 1.0
	v_div_scale_f32 v63, vcc, 1.0, v53, 1.0
	v_fmac_f32_e32 v66, v62, v66
	v_mul_f32_e32 v62, v63, v66
	v_fma_f32 v69, -v65, v62, v63
	v_fmac_f32_e32 v62, v69, v66
	v_fma_f32 v65, -v65, v62, v63
	v_div_fmas_f32 v65, v65, v66, v62
	v_div_fixup_f32 v65, v65, v53, 1.0
	v_cmp_lt_f32_e32 vcc, 0, v53
	v_or_b32_e32 v68, v68, v64
	s_nop 0
	v_cndmask_b32_e32 v62, 0, v65, vcc
	s_waitcnt vmcnt(0)
	v_pk_fma_f32 v[32:33], v[32:33], v[62:63], v[0:1] op_sel_hi:[1,0,1]
	v_pk_fma_f32 v[34:35], v[34:35], v[62:63], v[2:3] op_sel_hi:[1,0,1]
	v_pk_fma_f32 v[36:37], v[36:37], v[62:63], v[4:5] op_sel_hi:[1,0,1]
	v_pk_fma_f32 v[38:39], v[38:39], v[62:63], v[6:7] op_sel_hi:[1,0,1]
	v_cmp_gt_i32_e32 vcc, 0xc350, v49
	s_and_saveexec_b64 s[2:3], vcc
	global_store_dwordx4 v68, v[32:35], s[16:17] nt
	global_store_dwordx4 v68, v[36:39], s[16:17] offset:16 nt
	s_endpgm
